# rwkv step 2: CUM and AVs store addresses as two bases plus immediate offsets; step 2b scan addresses by one multiply-add and a stride
# speedup vs baseline: 1.0116x; 1.0008x over previous
.Lfp1_join:
	v_pk_add_f32 v[164:165], v[46:47], v[28:29] op_sel_hi:[1,0] neg_lo:[0,1] neg_hi:[0,1]
	v_pk_add_f32 v[174:175], v[44:45], v[36:37] op_sel_hi:[1,0] neg_lo:[0,1] neg_hi:[0,1]
	v_pk_add_f32 v[176:177], v[48:49], v[34:35] op_sel_hi:[1,0] neg_lo:[0,1] neg_hi:[0,1]
	ds_read_b128 v[44:47], v29
	ds_read_b128 v[48:51], v29 offset:256
	v_and_b32_e32 v78, 0xffff0000, v40
	v_pk_add_f32 v[150:151], v[150:151], v[78:79] op_sel_hi:[1,0] neg_lo:[0,1] neg_hi:[0,1]
	v_mul_lo_u32 v33, v142, s39
	s_waitcnt lgkmcnt(1)
	v_mov_b32_e32 v178, v44
	s_waitcnt lgkmcnt(0)
	v_mov_b32_e32 v179, v48
	v_mov_b32_e32 v48, v45
	v_pk_mul_f32 v[44:45], v[150:151], v[48:49]
	v_lshlrev_b32_e32 v80, 16, v41
	v_and_b32_e32 v82, 0xffff0000, v41
	v_lshlrev_b32_e32 v88, 16, v43
	v_add3_u32 v71, v111, v104, v33
	v_pk_add_f32 v[160:161], v[160:161], v[32:33] op_sel_hi:[1,0] neg_lo:[0,1] neg_hi:[0,1]
	v_add_f32_e32 v33, v44, v78
	v_pk_add_f32 v[152:153], v[152:153], v[80:81] op_sel_hi:[1,0] neg_lo:[0,1] neg_hi:[0,1]
	v_pk_add_f32 v[166:167], v[52:53], v[82:83] op_sel_hi:[1,0] neg_lo:[0,1] neg_hi:[0,1]
	v_pk_add_f32 v[168:169], v[56:57], v[84:85] op_sel_hi:[1,0] neg_lo:[0,1] neg_hi:[0,1]
	v_pk_add_f32 v[170:171], v[54:55], v[88:89] op_sel_hi:[1,0] neg_lo:[0,1] neg_hi:[0,1]
	v_pk_add_f32 v[172:173], v[58:59], v[60:61] op_sel_hi:[1,0] neg_lo:[0,1] neg_hi:[0,1]
	ds_read_b128 v[52:55], v29 offset:16
	ds_read_b128 v[56:59], v29 offset:272
	v_add_f32_e32 v33, v33, v45
	v_mov_b32_e32 v44, v46
	v_mov_b32_e32 v45, v50
	v_lshlrev_b32_e32 v76, 16, v40
	v_pk_mul_f32 v[44:45], v[152:153], v[44:45]
	v_pk_add_f32 v[148:149], v[148:149], v[76:77] op_sel_hi:[1,0] neg_lo:[0,1] neg_hi:[0,1]
	v_add_f32_e32 v35, v44, v80
	v_mov_b32_e32 v50, v47
	v_pk_mul_f32 v[148:149], v[148:149], v[178:179]
	v_add_f32_e32 v35, v35, v45
	v_pk_mul_f32 v[44:45], v[166:167], v[50:51]
	v_lshlrev_b32_e32 v40, 16, v37
	v_add_f32_e32 v29, v148, v76
	v_add_f32_e32 v37, v44, v82
	v_add_f32_e32 v29, v29, v149
	v_add_f32_e32 v37, v37, v45
	s_waitcnt lgkmcnt(1)
	v_mov_b32_e32 v44, v52
	s_waitcnt lgkmcnt(0)
	v_mov_b32_e32 v45, v56
	v_pk_mul_f32 v[44:45], v[168:169], v[44:45]
	v_add_f32_e32 v29, v29, v29
	v_pk_add_f32 v[154:155], v[154:155], v[86:87] op_sel_hi:[1,0] neg_lo:[0,1] neg_hi:[0,1]
	v_pk_add_f32 v[158:159], v[158:159], v[40:41] op_sel_hi:[1,0] neg_lo:[0,1] neg_hi:[0,1]
	v_add_f32_e32 v41, v44, v84
	v_mov_b32_e32 v56, v53
	v_mul_f32_e32 v29, 0x3fb8aa3b, v29
	v_add_f32_e32 v33, v33, v33
	v_add_f32_e32 v41, v41, v45
	v_pk_mul_f32 v[44:45], v[154:155], v[56:57]
	v_exp_f32_e32 v29, v29
	v_mul_f32_e32 v33, 0x3fb8aa3b, v33
	v_and_b32_e32 v90, 0xffff0000, v43
	v_pk_add_f32 v[156:157], v[156:157], v[42:43] op_sel_hi:[1,0] neg_lo:[0,1] neg_hi:[0,1]
	v_add_f32_e32 v43, v44, v86
	v_exp_f32_e32 v33, v33
	v_add_f32_e32 v43, v43, v45
	v_mov_b32_e32 v44, v54
	v_mov_b32_e32 v45, v58
	v_pk_mul_f32 v[44:45], v[170:171], v[44:45]
	v_add_f32_e32 v29, 1.0, v29
	v_add_f32_e32 v44, v44, v88
	v_add_f32_e32 v47, v44, v45
	v_rcp_f32_e32 v44, v29
	v_add_f32_e32 v29, 1.0, v33
	v_add_f32_e32 v33, v35, v35
	v_mul_f32_e32 v33, 0x3fb8aa3b, v33
	v_add_f32_e32 v35, v37, v37
	v_rcp_f32_e32 v45, v29
	v_exp_f32_e32 v33, v33
	v_mul_f32_e32 v35, 0x3fb8aa3b, v35
	v_pk_add_f32 v[38:39], v[38:39], v[90:91] op_sel_hi:[1,0] neg_lo:[0,1] neg_hi:[0,1]
	v_mov_b32_e32 v58, v55
	v_exp_f32_e32 v35, v35
	v_pk_mul_f32 v[38:39], v[38:39], v[58:59]
	v_add_f32_e32 v33, 1.0, v33
	v_add_f32_e32 v29, v38, v90
	v_add_f32_e32 v29, v29, v39
	v_pk_fma_f32 v[38:39], v[44:45], 2.0, 1.0 op_sel_hi:[1,0,0] neg_lo:[1,0,0] neg_hi:[1,0,0]
	v_add_f32_e32 v29, v29, v29
	v_cvt_pk_bf16_f32 v44, v38, v39
	v_rcp_f32_e32 v38, v33
	v_add_f32_e32 v33, 1.0, v35
	v_rcp_f32_e32 v39, v33
	v_add_f32_e32 v33, v41, v41
	v_mul_f32_e32 v33, 0x3fb8aa3b, v33
	v_add_f32_e32 v35, v43, v43
	v_exp_f32_e32 v33, v33
	v_mul_f32_e32 v35, 0x3fb8aa3b, v35
	v_exp_f32_e32 v35, v35
	v_mul_f32_e32 v29, 0x3fb8aa3b, v29
	v_add_f32_e32 v33, 1.0, v33
	v_rcp_f32_e32 v46, v33
	v_add_f32_e32 v33, 1.0, v35
	v_add_f32_e32 v35, v47, v47
	v_mul_f32_e32 v35, 0x3fb8aa3b, v35
	v_exp_f32_e32 v35, v35
	v_exp_f32_e32 v29, v29
	v_rcp_f32_e32 v47, v33
	v_pk_fma_f32 v[38:39], v[38:39], 2.0, 1.0 op_sel_hi:[1,0,0] neg_lo:[1,0,0] neg_hi:[1,0,0]
	v_add_f32_e32 v33, 1.0, v35
	v_add_f32_e32 v29, 1.0, v29
	v_rcp_f32_e32 v48, v33
	v_rcp_f32_e32 v49, v29
	v_cvt_pk_bf16_f32 v45, v38, v39
	v_pk_fma_f32 v[38:39], v[46:47], 2.0, 1.0 op_sel_hi:[1,0,0] neg_lo:[1,0,0] neg_hi:[1,0,0]
	v_add_u32_e32 v31, v118, v67
	v_cvt_pk_bf16_f32 v46, v38, v39
	v_pk_fma_f32 v[38:39], v[48:49], 2.0, 1.0 op_sel_hi:[1,0,0] neg_lo:[1,0,0] neg_hi:[1,0,0]
	s_lshl_b32 s0, s26, 10
	v_cvt_pk_bf16_f32 v47, v38, v39
	ds_write_b128 v71, v[44:47]
	ds_read_b128 v[44:47], v31
	ds_read_b128 v[48:51], v31 offset:256
	ds_read_b128 v[52:55], v31 offset:16
	ds_read_b128 v[56:59], v31 offset:272
	v_pk_add_f32 v[38:39], v[162:163], v[30:31] op_sel_hi:[1,0] neg_lo:[0,1] neg_hi:[0,1]
	s_or_b32 s28, s0, s5
	s_waitcnt lgkmcnt(3)
	v_mov_b32_e32 v76, v44
	s_waitcnt lgkmcnt(2)
	v_mov_b32_e32 v77, v48
	v_mov_b32_e32 v48, v45
	v_pk_mul_f32 v[44:45], v[156:157], v[48:49]
	v_mov_b32_e32 v43, v50
	v_add_f32_e32 v31, v44, v42
	v_mov_b32_e32 v42, v46
	v_pk_mul_f32 v[42:43], v[158:159], v[42:43]
	v_mov_b32_e32 v50, v47
	v_add_f32_e32 v44, v31, v45
	v_add_f32_e32 v31, v42, v40
	v_pk_mul_f32 v[40:41], v[174:175], v[50:51]
	v_add_f32_e32 v42, v31, v43
	v_add_f32_e32 v31, v40, v36
	s_waitcnt lgkmcnt(1)
	v_mov_b32_e32 v36, v52
	s_waitcnt lgkmcnt(0)
	v_mov_b32_e32 v37, v56
	v_pk_mul_f32 v[36:37], v[176:177], v[36:37]
	v_mov_b32_e32 v56, v53
	v_add_f32_e32 v40, v31, v41
	v_add_f32_e32 v31, v36, v34
	v_pk_mul_f32 v[34:35], v[160:161], v[56:57]
	v_add_f32_e32 v36, v31, v37
	v_add_f32_e32 v31, v34, v32
	v_mov_b32_e32 v32, v54
	v_mov_b32_e32 v33, v58
	v_pk_mul_f32 v[32:33], v[38:39], v[32:33]
	v_mov_b32_e32 v58, v55
	v_add_f32_e32 v30, v32, v30
	v_pk_mul_f32 v[76:77], v[172:173], v[76:77]
	v_add_f32_e32 v34, v31, v35
	v_add_f32_e32 v32, v30, v33
	v_pk_mul_f32 v[30:31], v[164:165], v[58:59]
	v_add_f32_e32 v29, v76, v60
	v_add_f32_e32 v28, v30, v28
	v_add_f32_e32 v29, v29, v77
	v_add_f32_e32 v31, v28, v31
	v_cvt_pk_bf16_f32 v28, v29, v44
	v_cvt_pk_bf16_f32 v29, v42, v40
	v_cvt_pk_bf16_f32 v30, v36, v34
	v_cvt_pk_bf16_f32 v31, v32, v31
	s_or_b32 s0, s41, s28
	s_mov_b32 s1, s29
	ds_write_b128 v71, v[28:31] offset:9216
	s_lshl_b64 s[0:1], s[0:1], 7
	v_and_b32_e32 v51, 15, v103
	v_lshrrev_b32_e32 v28, 1, v103
	s_add_u32 s60, s51, s0
	v_and_b32_e32 v50, 24, v28
	v_or_b32_e32 v48, s27, v51
	s_addc_u32 s61, s70, s1
	v_lshlrev_b32_e32 v44, 1, v50
	v_mov_b32_e32 v45, v105
	v_ashrrev_i32_e32 v49, 31, v48
	v_lshl_add_u64 v[28:29], s[60:61], 0, v[44:45]
	v_lshlrev_b64 v[30:31], 7, v[48:49]
	v_lshl_add_u64 v[32:33], v[28:29], 0, v[30:31]
	global_load_dwordx4 v[52:55], v[32:33], off
	global_load_dwordx4 v[56:59], v[32:33], off offset:64
	v_or_b32_e32 v49, s41, v51
	v_add_u32_e32 v32, s27, v49
	v_ashrrev_i32_e32 v33, 31, v32
	v_lshl_add_u64 v[32:33], v[32:33], 0, s[28:29]
	v_readlane_b32 s76, v253, 26
	v_lshlrev_b64 v[32:33], 2, v[32:33]
	v_readlane_b32 s90, v253, 40
	v_readlane_b32 s91, v253, 41
	s_add_u32 s0, s71, s0
	s_addc_u32 s1, s49, s1
	v_lshl_add_u64 v[34:35], s[90:91], 0, v[32:33]
	global_load_dword v60, v[34:35], off
	v_lshl_add_u64 v[34:35], s[0:1], 0, v[44:45]
	v_lshl_add_u64 v[30:31], v[34:35], 0, v[30:31]
	global_load_dwordx4 v[76:79], v[30:31], off
	global_load_dwordx4 v[80:83], v[30:31], off offset:64
	v_readlane_b32 s77, v253, 27
	v_readlane_b32 s78, v253, 28
	v_readlane_b32 s79, v253, 29
	v_readlane_b32 s80, v253, 30
	v_readlane_b32 s81, v253, 31
	v_readlane_b32 s82, v253, 32
	v_readlane_b32 s83, v253, 33
	v_readlane_b32 s84, v253, 34
	v_readlane_b32 s85, v253, 35
	v_readlane_b32 s86, v253, 36
	v_readlane_b32 s87, v253, 37
	v_readlane_b32 s72, v253, 42
	v_readlane_b32 s74, v253, 44
	v_readlane_b32 s75, v253, 45
	v_or_b32_e32 v46, s63, v51
	v_ashrrev_i32_e32 v47, 31, v46
	v_lshl_add_u64 v[30:31], s[74:75], 0, v[32:33]
	global_load_dword v71, v[30:31], off
	v_lshlrev_b64 v[30:31], 7, v[46:47]
	v_lshl_add_u64 v[28:29], v[28:29], 0, v[30:31]
	v_lshl_add_u64 v[30:31], v[34:35], 0, v[30:31]
	global_load_dwordx4 v[84:87], v[28:29], off
	global_load_dwordx4 v[88:91], v[28:29], off offset:64
	global_load_dwordx4 v[148:151], v[30:31], off
	global_load_dwordx4 v[152:155], v[30:31], off offset:64
	v_add_u32_e32 v156, s63, v49
	s_lshl_b32 s41, s41, 2
	v_ashrrev_i32_e32 v157, 31, v156
	v_or_b32_e32 v45, s34, v51
	s_add_u32 s0, s42, s41
	v_lshl_add_u64 v[156:157], v[156:157], 0, s[28:29]
	v_mul_u32_u24_e32 v45, 0x48, v45
	s_addc_u32 s1, s36, 0
	v_lshlrev_b64 v[156:157], 2, v[156:157]
	v_lshlrev_b32_e32 v45, 1, v45
	s_add_u32 s60, s52, s41
	v_lshl_add_u64 v[158:159], s[90:91], 0, v[156:157]
	v_lshl_add_u64 v[156:157], s[74:75], 0, v[156:157]
	v_add3_u32 v45, v111, v45, v44
	s_addc_u32 s61, s53, 0
	global_load_dwordx4 v[32:35], v67, s[0:1] offset:16
	global_load_dwordx4 v[40:43], v67, s[0:1]
	global_load_dwordx4 v[28:31], v67, s[60:61] offset:16
	global_load_dwordx4 v[36:39], v67, s[60:61]
	global_load_dword v75, v[156:157], off
	s_mov_b32 s0, 0xbfb8aa3b
	global_load_dword v67, v[158:159], off
	s_waitcnt lgkmcnt(0)
	s_barrier
	ds_read_b128 v[156:159], v45
	ds_read_b128 v[160:163], v45 offset:64
	s_waitcnt vmcnt(15) lgkmcnt(1)
	v_mfma_f32_16x16x32_bf16 v[52:55], v[156:159], v[52:55], 0
	ds_read_b128 v[164:167], v45 offset:9216
	s_movk_i32 s1, 0x41
	v_and_b32_e32 v49, 63, v103
	s_waitcnt vmcnt(14) lgkmcnt(1)
	v_mfma_f32_16x16x32_bf16 v[52:55], v[160:163], v[56:59], v[52:55]
	v_readlane_b32 s88, v253, 38
	v_readlane_b32 s89, v253, 39
	v_readlane_b32 s73, v253, 43
	v_readlane_b32 s76, v253, 46
	v_readlane_b32 s77, v253, 47
	v_readlane_b32 s78, v253, 48
	v_readlane_b32 s79, v253, 49
	v_readlane_b32 s80, v253, 50
	s_waitcnt vmcnt(13)
	v_add_f32_e32 v52, v60, v52
	v_mul_f32_e64 v47, |v52|, s0
	v_exp_f32_e32 v56, v47
	v_lshrrev_b32_e32 v47, 2, v103
	v_add_f32_e32 v53, v60, v53
	v_add_f32_e32 v54, v60, v54
	v_add_f32_e32 v56, 1.0, v56
	v_log_f32_e32 v147, v56
	ds_read_b128 v[56:59], v45 offset:9280
	s_waitcnt vmcnt(12) lgkmcnt(1)
	v_mfma_f32_16x16x32_bf16 v[76:79], v[164:167], v[76:79], 0
	v_max_f32_e64 v45, -v52, 0
	v_fmac_f32_e32 v45, 0x3f317218, v147
	v_sub_f32_e32 v45, -0.5, v45
	s_waitcnt vmcnt(11) lgkmcnt(0)
	v_mfma_f32_16x16x32_bf16 v[76:79], v[56:59], v[80:83], v[76:79]
	v_mul_f32_e32 v45, 0x3fb8aa3b, v45
	v_exp_f32_e32 v52, v45
	v_and_b32_e32 v45, 12, v47
	s_waitcnt vmcnt(10)
	s_nop 3
	v_add_f32_e32 v76, v71, v76
	v_mul_f32_e32 v76, 0xbfb8aa3b, v76
	v_exp_f32_e32 v76, v76
	v_or_b32_e32 v147, s34, v45
	v_mul_u32_u24_e32 v80, 0x41, v147
	v_add_lshl_u32 v218, v80, v48, 2
	v_add_f32_e32 v76, 1.0, v76
	v_rcp_f32_e32 v76, v76
	v_mul_f32_e64 v82, |v53|, s0
	v_xor_b32_e32 v52, 0x80000000, v52
	v_exp_f32_e32 v82, v82
	v_add_u32_e32 v218, v113, v218
	ds_write_b32 v218, v52
	ds_write_b32 v218, v76 offset:16640
	v_add_f32_e32 v76, v71, v77
	v_mul_f32_e64 v77, |v54|, s0
	v_exp_f32_e32 v77, v77
	v_add_f32_e32 v82, 1.0, v82
	v_log_f32_e32 v82, v82
	v_max_f32_e64 v53, -v53, 0
	v_add_f32_e32 v77, 1.0, v77
	v_log_f32_e32 v77, v77
	v_fmac_f32_e32 v53, 0x3f317218, v82
	v_mul_f32_e32 v76, 0xbfb8aa3b, v76
	v_sub_f32_e32 v53, -0.5, v53
	v_exp_f32_e32 v76, v76
	v_mul_f32_e32 v53, 0x3fb8aa3b, v53
	v_max_f32_e64 v54, -v54, 0
	v_exp_f32_e32 v53, v53
	v_fmac_f32_e32 v54, 0x3f317218, v77
	v_sub_f32_e32 v54, -0.5, v54
	v_add_f32_e32 v55, v60, v55
	v_add_f32_e32 v76, 1.0, v76
	v_mul_f32_e32 v54, 0x3fb8aa3b, v54
	v_mul_f32_e64 v60, |v55|, s0
	v_rcp_f32_e32 v76, v76
	v_exp_f32_e32 v54, v54
	v_exp_f32_e32 v60, v60
	v_xor_b32_e32 v52, 0x80000000, v53
	ds_write_b32 v218, v52 offset:260
	ds_write_b32 v218, v76 offset:16900
	v_xor_b32_e32 v52, 0x80000000, v54
	v_add_f32_e32 v54, v71, v78
	v_add_f32_e32 v60, 1.0, v60
	v_mul_f32_e32 v54, 0xbfb8aa3b, v54
	v_log_f32_e32 v60, v60
	v_exp_f32_e32 v54, v54
	v_max_f32_e64 v55, -v55, 0
	v_fmac_f32_e32 v55, 0x3f317218, v60
	v_add_f32_e32 v54, 1.0, v54
	v_sub_f32_e32 v55, -0.5, v55
	v_rcp_f32_e32 v54, v54
	v_mul_f32_e32 v55, 0x3fb8aa3b, v55
	v_exp_f32_e32 v55, v55
	ds_write_b32 v218, v52 offset:520
	ds_write_b32 v218, v54 offset:17160
	v_xor_b32_e32 v60, 0x80000000, v55
	s_waitcnt vmcnt(9)
	v_mfma_f32_16x16x32_bf16 v[52:55], v[156:159], v[84:87], 0
	v_add_f32_e32 v71, v71, v79
	v_mul_f32_e32 v71, 0xbfb8aa3b, v71
	v_exp_f32_e32 v71, v71
	s_waitcnt vmcnt(8)
	v_mfma_f32_16x16x32_bf16 v[52:55], v[160:163], v[88:91], v[52:55]
	ds_write_b32 v218, v60 offset:780
	v_add_f32_e32 v60, 1.0, v71
	v_rcp_f32_e32 v60, v60
	s_waitcnt vmcnt(0)
	s_nop 1
	v_add_f32_e32 v52, v67, v52
	v_mul_f32_e64 v77, |v52|, s0
	v_exp_f32_e32 v77, v77
	v_add_f32_e32 v53, v67, v53
	v_max_f32_e64 v52, -v52, 0
	v_add_f32_e32 v71, 1.0, v77
	v_mfma_f32_16x16x32_bf16 v[76:79], v[164:167], v[148:151], 0
	v_log_f32_e32 v71, v71
	ds_write_b32 v218, v60 offset:17420
	v_mul_f32_e64 v60, |v53|, s0
	v_mfma_f32_16x16x32_bf16 v[56:59], v[56:59], v[152:155], v[76:79]
	v_fmac_f32_e32 v52, 0x3f317218, v71
	v_exp_f32_e32 v60, v60
	v_sub_f32_e32 v52, -0.5, v52
	v_mul_f32_e32 v52, 0x3fb8aa3b, v52
	v_exp_f32_e32 v52, v52
	s_nop 2
	v_add_f32_e32 v56, v75, v56
	v_mul_f32_e32 v56, 0xbfb8aa3b, v56
	v_exp_f32_e32 v56, v56
	v_add_f32_e32 v60, 1.0, v60
	v_log_f32_e32 v60, v60
	v_xor_b32_e32 v48, 0x80000000, v52
	v_add_f32_e32 v56, 1.0, v56
	v_rcp_f32_e32 v56, v56
	v_add_lshl_u32 v219, v80, v46, 2
	v_add_u32_e32 v219, v113, v219
	v_max_f32_e64 v53, -v53, 0
	v_fmac_f32_e32 v53, 0x3f317218, v60
	ds_write_b32 v219, v48
	v_add_f32_e32 v54, v67, v54
	v_sub_f32_e32 v53, -0.5, v53
	ds_write_b32 v219, v56 offset:16640
	v_mul_f32_e64 v56, |v54|, s0
	v_mul_f32_e32 v53, 0x3fb8aa3b, v53
	v_exp_f32_e32 v56, v56
	v_exp_f32_e32 v53, v53
	v_max_f32_e64 v54, -v54, 0
	v_add_f32_e32 v56, 1.0, v56
	v_xor_b32_e32 v48, 0x80000000, v53
	v_add_f32_e32 v53, v75, v57
	v_log_f32_e32 v56, v56
	v_mul_f32_e32 v53, 0xbfb8aa3b, v53
	v_exp_f32_e32 v53, v53
	v_fmac_f32_e32 v54, 0x3f317218, v56
	v_sub_f32_e32 v54, -0.5, v54
	v_add_f32_e32 v53, 1.0, v53
	v_mul_f32_e32 v54, 0x3fb8aa3b, v54
	v_rcp_f32_e32 v53, v53
	v_exp_f32_e32 v54, v54
	ds_write_b32 v219, v48 offset:260
	ds_write_b32 v219, v53 offset:16900
	v_xor_b32_e32 v48, 0x80000000, v54
	v_add_f32_e32 v53, v75, v58
	v_add_f32_e32 v54, v67, v55
	v_mul_f32_e32 v53, 0xbfb8aa3b, v53
	v_mul_f32_e64 v55, |v54|, s0
	v_exp_f32_e32 v53, v53
	v_exp_f32_e32 v55, v55
	ds_write_b32 v219, v48 offset:520
	v_add_f32_e32 v48, 1.0, v53
	v_add_f32_e32 v53, 1.0, v55
	v_log_f32_e32 v53, v53
	v_max_f32_e64 v54, -v54, 0
	v_rcp_f32_e32 v48, v48
	v_fmac_f32_e32 v54, 0x3f317218, v53
	v_sub_f32_e32 v53, -0.5, v54
	v_mul_f32_e32 v53, 0x3fb8aa3b, v53
	v_exp_f32_e32 v53, v53
	v_add_f32_e32 v54, v75, v59
	v_mul_f32_e32 v54, 0xbfb8aa3b, v54
	v_exp_f32_e32 v54, v54
	ds_write_b32 v219, v48 offset:17160
	v_xor_b32_e32 v48, 0x80000000, v53
	ds_write_b32 v219, v48 offset:780
	v_ashrrev_i32_e32 v48, 6, v103
	v_add_f32_e32 v52, 1.0, v54
	v_lshlrev_b32_e32 v59, 3, v48
	v_rcp_f32_e32 v52, v52
	v_sub_u32_e32 v53, 63, v59
	v_lshlrev_b32_e32 v46, 2, v49
	v_cndmask_b32_e64 v53, v53, v59, s[12:13]
	ds_write_b32 v219, v52 offset:17420
	s_movk_i32 s0, 0x104
	v_add_u32_e32 v60, v113, v46
	v_mov_b32_e32 v216, 0xfffffefc
	v_mov_b32_e32 v217, 0x104
	v_mad_u32_u24 v52, v53, s0, v60
	v_cndmask_b32_e64 v216, v216, v217, s[12:13]
	s_waitcnt lgkmcnt(0)
	s_barrier
	v_add_u32_e32 v53, v52, v216
	v_add_u32_e32 v54, v53, v216
	v_add_u32_e32 v55, v54, v216
	v_add_u32_e32 v56, v55, v216
	v_add_u32_e32 v57, v56, v216
	v_add_u32_e32 v58, v57, v216
	v_add_u32_e32 v59, v58, v216
	ds_read_b32 v60, v52
	ds_read_b32 v67, v53
	ds_read_b32 v71, v54
	ds_read_b32 v75, v55
	ds_read_b32 v80, v56
	ds_read_b32 v81, v57
	ds_read_b32 v82, v58
	ds_read_b32 v83, v59
	s_waitcnt lgkmcnt(7)
	v_add_f32_e32 v79, 0, v60
	s_waitcnt lgkmcnt(6)
	v_add_f32_e32 v78, v79, v67
	s_waitcnt lgkmcnt(5)
	v_add_f32_e32 v77, v78, v71
	s_waitcnt lgkmcnt(4)
	v_add_f32_e32 v76, v77, v75
	s_waitcnt lgkmcnt(3)
	v_add_f32_e32 v75, v76, v80
	s_waitcnt lgkmcnt(2)
	v_add_f32_e32 v71, v75, v81
	s_waitcnt lgkmcnt(1)
	v_add_f32_e32 v67, v71, v82
	s_waitcnt lgkmcnt(0)
	v_add_f32_e32 v60, v67, v83
	v_lshl_add_u32 v80, v103, 2, v120
	ds_write_b32 v80, v60
	v_add_u32_e32 v81, v120, v46
	v_cmp_lt_i32_e32 vcc, 0, v48
	v_mov_b32_e32 v80, 0
	v_readlane_b32 s81, v253, 51
	v_readlane_b32 s82, v253, 52
	v_readlane_b32 s83, v253, 53
	v_readlane_b32 s84, v253, 54
	v_readlane_b32 s85, v253, 55
	v_readlane_b32 s86, v253, 56
	v_readlane_b32 s87, v253, 57
	s_waitcnt lgkmcnt(0)
	s_barrier
	ds_read_b32 v216, v81
	ds_read_b32 v217, v81 offset:256
	ds_read_b32 v218, v81 offset:512
	ds_read_b32 v219, v81 offset:768
	ds_read_b32 v220, v81 offset:1024
	ds_read_b32 v221, v81 offset:1280
	ds_read_b32 v222, v81 offset:1536
	v_readfirstlane_b32 s0, v48
	s_movk_i32 s75, 0xfc0
	s_waitcnt lgkmcnt(0)
	s_cmp_lt_i32 s0, 1
	s_cbranch_scc1 .Lseg_done
	v_add_f32_e32 v80, 0, v216
	s_cmp_lt_i32 s0, 2
	s_cbranch_scc1 .Lseg_done
	v_add_f32_e32 v80, v80, v217
	s_cmp_lt_i32 s0, 3
	s_cbranch_scc1 .Lseg_done
	v_add_f32_e32 v80, v80, v218
	s_cmp_lt_i32 s0, 4
	s_cbranch_scc1 .Lseg_done
	v_add_f32_e32 v80, v80, v219
	s_cmp_lt_i32 s0, 5
	s_cbranch_scc1 .Lseg_done
	v_add_f32_e32 v80, v80, v220
	s_cmp_lt_i32 s0, 6
	s_cbranch_scc1 .Lseg_done
	v_add_f32_e32 v80, v80, v221
	s_cmp_lt_i32 s0, 7
	s_cbranch_scc1 .Lseg_done
	v_add_f32_e32 v80, v80, v222
